# final6 + LDS bank-conflict swizzle for the diff-attention K image: row swizzle (row&7)<<4 -> (row&15)<<4 (K-staging waves XOR 0x80 into the source column of DMA pieces holding rows 8-15; K read mask 0
# speedup vs baseline: 1.0136x; 1.0136x over previous
; #define LAS __attribute__((address_space(3)))
; #define AT_BAR() asm volatile("s_waitcnt vmcnt(0) lgkmcnt(0)\n\ts_barrier" ::: "memory")
; DI void at_stage1(LAS unsigned char* lds, const char* projb, int kcolB, int vcolB, int kt, int slot, int wid, unsigned lb0, unsigned lb1) {
;     const int kv = wid >> 2, sub0 = (wid & 3) * 4;
;     LAS unsigned char* dst = lds + slot * 32768 + kv * 16384 + sub0 * 1024;
;     const char* tb = projb + (size_t)kt * 64 * (INW * 2) + (kv ? vcolB : kcolB);
; #pragma unroll
;     for (int n = 0; n < 4; ++n) { const int sub = sub0 + n;
;         const size_t U = kv ? (size_t)((sub >> 1) * 8) * (INW * 2) + (size_t)((sub & 1) * 128) : (size_t)(sub * 4) * (INW * 2);
;         __builtin_amdgcn_global_load_lds((const unsigned*)(tb + U + ((n & 1) ? lb1 : lb0)), (LAS unsigned*)(dst + n * 1024), 16, 0, 0); }
; }
; DI void attn_unit_diff(const Ctx& C, int l, int b, int h, int j) {
;     ...
;     AT_BAR();
;     unsigned lb0, lb1;
;     { const int kv = wid >> 2;
;       if (kv == 0) { const int rl = lane >> 4, cp = lane & 15; lb0 = (unsigned)(rl * (INW * 2) + ((cp ^ (rl & 7)) * 16)); lb1 = (unsigned)(rl * (INW * 2) + ((cp ^ ((4 + rl) & 7)) * 16)); }
;       else { lb0 = (unsigned)(((lane & 31) >> 2) * (INW * 2) + ((lane >> 5) * 32 + (lane & 3) * 8) * 2); lb1 = lb0; } }
;     at_stage1(C.lds, projb, kcolB, vcolB, 0, 0, wid, lb0, lb1);
;     at_stage1(C.lds, projb, kcolB, vcolB, 1, 1, wid, lb0, lb1);
;     __builtin_amdgcn_sched_barrier(0);
;     bf16x8 qr[8];
;     { const bf16_t* qp = proj + (rowb + qpos) * INW + qcol + 8 * hi;
; #pragma unroll
;       for (int s = 0; s < KS; ++s) qr[s] = *(const bf16x8*)(qp + 16 * s); }
;     for (int i = wid * 64 + lane; i < TABB_N; i += NTHREADS) tabl[i] = tabg[i];
.LBB0_773:
	v_mov_b32_e32 v154, v153
	s_waitcnt vmcnt(0) lgkmcnt(0)
	s_barrier
	v_readlane_b32 s6, v252, 24
	v_readlane_b32 s7, v252, 25
	v_and_b32_e32 v155, 31, v154
	s_mov_b64 s[38:39], -1
	s_and_b64 vcc, exec, s[6:7]
	s_waitcnt vmcnt(0)
	v_lshlrev_b32_e32 v8, 3, v154
	s_cbranch_vccz .LBB0_775
	v_lshrrev_b32_e32 v0, 2, v155
	v_and_b32_e32 v2, 0x7fffffe0, v154
	s_mov_b32 s101, 0
	v_mul_u32_u24_e32 v0, 0x3000, v0
	v_and_or_b32 v2, v8, 24, v2
	v_lshl_add_u32 v2, v2, 1, v0
	s_mov_b64 s[38:39], 0
.LBB0_775:
	s_movk_i32 s48, 0x2800
	s_andn2_b64 vcc, exec, s[38:39]
	v_readlane_b32 s40, v252, 31
	v_readlane_b32 s41, v252, 30
	v_mov_b32_e32 v0, v2
	s_cbranch_vccnz .LBB0_777
	v_ashrrev_i32_e32 v0, 4, v154
	v_and_b32_e32 v2, 15, v154
	v_mul_lo_u32 v3, v0, s17
	s_movk_i32 s101, 0x80
	v_bitop3_b32 v0, v0, v2, 7 bitop3:0x6c
	v_lshlrev_b32_e32 v2, 4, v0
	v_or_b32_e32 v0, v2, v3
	v_bitop3_b32 v2, v2, 64, v3 bitop3:0x36
	s_movk_i32 s48, 0x2000
	v_readlane_b32 s40, v252, 32
	v_readlane_b32 s41, v252, 29
.LBB0_777:
	s_bfe_u32 s11, s97, 0x30004
	s_ashr_i32 s38, s97, 7
	s_and_b32 s6, s97, 15
	s_lshl_b32 s54, s11, 7
	v_readlane_b32 s15, v252, 21
	s_ashr_i32 s39, s38, 31
	s_mul_i32 s7, s11, 0xa00
	s_xor_b32 s49, s6, 31
	s_add_i32 s28, s15, s54
	s_lshl_b32 s11, s11, 8
	s_lshl_b64 s[74:75], s[38:39], 12
	s_mul_i32 s42, s38, 0x3000000
	s_mul_hi_i32 s43, s38, 0x3000000
	s_add_u32 s15, s46, s42
	s_addc_u32 s16, s47, s43
	s_lshl_b32 s52, s49, 7
	v_readlane_b32 s31, v252, 23
	s_or_b32 s55, s52, s31
	s_add_u32 s76, s92, s7
	s_addc_u32 s77, s23, 0
	s_or_b32 s50, s48, s11
	s_add_u32 s31, s15, s50
	s_addc_u32 s35, s16, 0
	s_add_u32 s38, s31, s21
	v_readlane_b32 s57, v253, 58
	s_addc_u32 s39, s35, 0
	s_mov_b32 m0, s57
	v_lshl_add_u64 v[4:5], s[38:39], 0, v[0:1]
	global_load_lds_dwordx4 v0, s[38:39]
	s_add_u32 s38, s31, s41
	s_addc_u32 s39, s35, 0
	s_add_i32 s82, s57, 0x400
	s_mov_b32 m0, s82
	s_add_i32 s83, s57, 0x800
	global_load_lds_dwordx4 v2, s[38:39]
	s_add_u32 s38, s31, s40
	s_addc_u32 s39, s35, 0
	s_add_i32 s84, s57, 0xc00
	s_add_u32 s31, s15, 0xc0000
	s_mov_b64 s[66:67], 0x18000
	s_addc_u32 s35, s16, 0
	v_lshl_add_u64 v[4:5], v[4:5], 0, s[66:67]
	s_mov_b32 m0, s83
	s_add_u32 s50, s31, s50
	s_mov_b32 s58, s57
	v_xor_b32_e32 v4, s101, v4
	global_load_lds_dwordx4 v[4:5], off
	s_mov_b32 m0, s84
	s_addc_u32 s57, s35, 0
	v_xor_b32_e32 v6, s101, v2
	global_load_lds_dwordx4 v6, s[38:39]
	s_add_u32 s38, s50, s21
	s_addc_u32 s39, s57, 0
	s_add_i32 s85, s58, 0x8000
	s_mov_b32 m0, s85
	v_lshl_add_u64 v[4:5], s[38:39], 0, v[0:1]
	global_load_lds_dwordx4 v0, s[38:39]
	s_add_u32 s38, s50, s41
	s_addc_u32 s39, s57, 0
	s_add_i32 s86, s58, 0x8400
	s_mov_b32 m0, s86
	s_add_i32 s87, s58, 0x8800
	global_load_lds_dwordx4 v2, s[38:39]
	s_add_u32 s38, s50, s40
	v_lshl_add_u64 v[4:5], v[4:5], 0, s[66:67]
	s_mov_b32 m0, s87
	s_addc_u32 s39, s57, 0
	s_add_i32 s93, s58, 0x8c00
	v_xor_b32_e32 v4, s101, v4
	global_load_lds_dwordx4 v[4:5], off
	s_mov_b32 m0, s93
	v_ashrrev_i32_e32 v156, 5, v154
	v_xor_b32_e32 v6, s101, v2
	global_load_lds_dwordx4 v6, s[38:39]
	v_or_b32_e32 v3, s55, v155
	v_or_b32_e32 v3, s74, v3
	v_mov_b64_e32 v[4:5], s[46:47]
	v_mad_u64_u32 v[4:5], s[38:39], v3, s17, v[4:5]
	v_mad_i32_i24 v5, s75, v195, v5
	s_lshl_b32 s78, s28, 1
	s_mov_b32 s79, s53
	v_lshlrev_b32_e32 v144, 3, v156
	v_lshl_add_u64 v[4:5], v[4:5], 0, s[78:79]
	v_ashrrev_i32_e32 v145, 31, v144
	v_lshl_add_u64 v[4:5], v[144:145], 1, v[4:5]
	global_load_dwordx4 v[128:131], v[4:5], off
	global_load_dwordx4 v[132:135], v[4:5], off offset:32
	global_load_dwordx4 v[136:139], v[4:5], off offset:64
	global_load_dwordx4 v[140:143], v[4:5], off offset:96
	v_readlane_b32 s28, v251, 4
	s_nop 1
	v_add_u32_e32 v4, s28, v154
	s_movk_i32 s28, 0x280
	v_cmp_gt_i32_e32 vcc, s28, v4
	s_and_saveexec_b64 s[38:39], vcc
	s_cbranch_execz .LBB0_785
	v_max_i32_e32 v3, 0x80, v4
	v_sub_u32_e32 v3, v3, v4
	v_add_u32_e32 v3, 0x1ff, v3
	s_movk_i32 s28, 0x1ff
	v_cmp_lt_u32_e32 vcc, s28, v3
	s_mov_b64 s[58:59], -1
	s_and_saveexec_b64 s[40:41], vcc
	s_cbranch_execz .LBB0_782
	v_lshrrev_b32_e32 v3, 9, v3
	v_add_u32_e32 v3, 1, v3
	v_and_b32_e32 v9, 0xfffffe, v3
	v_add_u32_e32 v5, 0x200, v4
	v_readlane_b32 s28, v253, 22
	s_mov_b64 s[58:59], 0
	v_mov_b32_e32 v11, v9
	v_lshl_add_u32 v10, v154, 2, s28
	v_mov_b64_e32 v[6:7], v[4:5]

; #define LAS __attribute__((address_space(3)))
;     __device__ __forceinline__ void init(const void* A_, const void* B_, int lda_, int ldb_, int M, unsigned mask_, int G_, int c_) { A = (const char*)A_; B = (const char*)B_; lda = lda_; ldb = ldb_; nM = M / BM; mask = mask_; nN = __builtin_popcount(mask_); nwg = nM * nN; G = G_; c = c_; }
;     __device__ __forceinline__ void init(f32x4 (&acc)[2][2][4][2], const Unit& u, int wr, int wc, int fr, int fq) const { u32x4 old[2][4][2]; init_load(old, u, wr, wc, fr, fq); init_finish(acc, old); }
; DI int at_v_rd_base(int lane) { return ((lane & 3) << 3) | (((lane >> 2) & 3) << 6) | (((lane >> 4) & 1) << 5) | (((lane >> 5) & 1) << 8); }
; template <int OFF> DI s16x4 at_tr_read(int vb) { s16x4 r; asm volatile("ds_read_b64_tr_b16 %0, %1 offset:%2" : "=&v"(r) : "v"(vb), "i"(OFF) : "memory"); return r; }
; DI unsigned at_cvtpk(float lo, float hi) { unsigned r; asm volatile("v_cvt_pk_bf16_f32 %0, %1, %2" : "=v"(r) : "v"(lo), "v"(hi)); return r; }
; template <int KS> DI void at_qk(f32x16& p0, f32x16& p1, LAS const unsigned char* Kt, int mapB, const bf16x8 (&qr)[8], float init, int r32, int hi) {
; #pragma unroll
;     for (int i = 0; i < 16; ++i) { p0[i] = init; p1[i] = init; }
;     bf16x8 kb[KS][2];
; #pragma unroll
;     for (int d0 = 0; d0 < KS; ++d0) { const int cb = mapB + (d0 * 16 + hi * 8) * 2;
;         kb[d0][0] = *(const LAS bf16x8*)(Kt + AT_KSWZ(r32, cb)); kb[d0][1] = *(const LAS bf16x8*)(Kt + AT_KSWZ(32 + r32, cb)); }
; DI void attn_unit_diff(const Ctx& C, int l, int b, int h, int j) {
;     ...
;     f32x16 o[4], ol = {}; float m_run = 0.f; bool first = true;
; #pragma unroll
;     for (int d0 = 0; d0 < 4; ++d0) o[d0] = f32x16{};
;     const bf16x8 ones = {16256, 16256, 16256, 16256, 16256, 16256, 16256, 16256};
;     asm volatile("s_waitcnt vmcnt(0) lgkmcnt(0)\n\ts_barrier" ::: "memory");
;     const float cfar = tabl[0];
;     const int vrd = at_v_rd_base(lane);
;     for (int sd = 0; sd < nt; ++sd) {
;         const int slot = sd % 3;
.LBB0_785:
	s_or_b64 exec, exec, s[38:39]
	s_add_i32 s50, 0, 0x20000
	s_lshr_b32 s28, s97, 4
	s_lshl_b32 s66, s49, 1
	v_readlane_b32 s38, v252, 22
	s_waitcnt vmcnt(0) lgkmcnt(0)
	s_barrier
	v_mov_b32_e32 v4, s50
	s_and_b32 s28, s28, 7
	s_or_b32 s67, s66, s38
	s_waitcnt lgkmcnt(0)
	ds_read_b32 v158, v4
	v_and_b32_e32 v4, 24, v8
	v_and_b32_e32 v7, 0x100, v8
	v_lshlrev_b32_e32 v8, 4, v156
	v_readlane_b32 s38, v252, 26
	s_lshl_b32 s28, s28, 8
	v_lshlrev_b32_e32 v145, 4, v154
	v_add_u32_e32 v9, s38, v8
	v_readlane_b32 s38, v252, 23
	v_lshlrev_b32_e32 v11, 4, v155
	v_lshlrev_b32_e32 v15, 2, v154
	s_add_i32 s88, s55, 0xfffffe90
	s_add_i32 s38, s38, s52
	s_add_i32 s91, 0, 0x4000
	s_add_i32 s52, s48, s28
	v_mov_b32_e32 v3, v1
	v_and_b32_e32 v5, 0xc0, v145
	v_lshlrev_b32_e32 v6, 1, v154
	v_lshlrev_b32_e32 v10, 8, v155
	v_and_b32_e32 v11, 0xf0, v11
	v_add_u32_e32 v14, 0x60, v9
	v_xor_b32_e32 v157, 0x80, v15
	v_add_lshl_u32 v15, s38, v155, 2
	s_add_u32 s38, s96, s42
	v_and_b32_e32 v6, 32, v6
	v_add_u32_e32 v12, 32, v9
	v_add_u32_e32 v13, 64, v9
	v_sub_u32_e32 v159, v8, v15
	v_add3_u32 v5, v7, s91, v5
	v_xad_u32 v164, v14, v11, v10
	v_lshl_add_u64 v[2:3], s[42:43], 0, v[2:3]
	s_addc_u32 s39, s89, s43
	v_mov_b32_e32 v14, v1
	v_mov_b32_e32 v15, v1
	v_add3_u32 v160, v5, v6, v4
	v_xad_u32 v161, v9, v11, v10
	v_xad_u32 v162, v12, v11, v10
	v_xad_u32 v163, v13, v11, v10
	v_lshl_add_u64 v[146:147], s[70:71], 0, v[2:3]
	v_lshl_add_u64 v[148:149], s[72:73], 0, v[2:3]
	v_lshl_add_u64 v[150:151], s[38:39], 0, v[0:1]
	s_lshl_b32 s95, s49, 16
	v_mov_b32_e32 v0, v1
	v_mov_b32_e32 v2, v1
	v_mov_b32_e32 v3, v1
	v_mov_b32_e32 v4, v1
	v_mov_b32_e32 v5, v1
	v_mov_b32_e32 v6, v1
	v_mov_b32_e32 v7, v1
	v_mov_b32_e32 v8, v1
	v_mov_b32_e32 v9, v1
	v_mov_b32_e32 v10, v1
	v_mov_b32_e32 v11, v1
	v_mov_b32_e32 v12, v1
	v_mov_b32_e32 v13, v1
	v_mov_b64_e32 v[78:79], v[14:15]
	v_mov_b64_e32 v[62:63], v[14:15]
	v_mov_b64_e32 v[46:47], v[14:15]
	v_mov_b64_e32 v[30:31], v[14:15]
	v_mov_b64_e32 v[94:95], v[14:15]
	s_mov_b32 s79, 2
	s_add_i32 s95, s95, 0x10000
	s_mov_b32 s48, 0
	v_mov_b32_e32 v165, 0
	s_mov_b64 s[38:39], -1
	s_mov_b32 s49, 0
	v_mov_b64_e32 v[76:77], v[12:13]
	v_mov_b64_e32 v[74:75], v[10:11]
	v_mov_b64_e32 v[72:73], v[8:9]
	v_mov_b64_e32 v[70:71], v[6:7]
	v_mov_b64_e32 v[68:69], v[4:5]
	v_mov_b64_e32 v[66:67], v[2:3]
	v_mov_b64_e32 v[64:65], v[0:1]
	v_mov_b64_e32 v[60:61], v[12:13]
	v_mov_b64_e32 v[58:59], v[10:11]
	v_mov_b64_e32 v[56:57], v[8:9]
	v_mov_b64_e32 v[54:55], v[6:7]
	v_mov_b64_e32 v[52:53], v[4:5]
	v_mov_b64_e32 v[50:51], v[2:3]
	v_mov_b64_e32 v[48:49], v[0:1]
	v_mov_b64_e32 v[44:45], v[12:13]
	v_mov_b64_e32 v[42:43], v[10:11]
	v_mov_b64_e32 v[40:41], v[8:9]
	v_mov_b64_e32 v[38:39], v[6:7]
	v_mov_b64_e32 v[36:37], v[4:5]
	v_mov_b64_e32 v[34:35], v[2:3]
	v_mov_b64_e32 v[32:33], v[0:1]
	v_mov_b64_e32 v[28:29], v[12:13]
	v_mov_b64_e32 v[26:27], v[10:11]
	v_mov_b64_e32 v[24:25], v[8:9]
	v_mov_b64_e32 v[22:23], v[6:7]
	v_mov_b64_e32 v[20:21], v[4:5]
	v_mov_b64_e32 v[18:19], v[2:3]
	v_mov_b64_e32 v[16:17], v[0:1]
	v_mov_b64_e32 v[92:93], v[12:13]
	v_mov_b64_e32 v[90:91], v[10:11]
	v_mov_b64_e32 v[88:89], v[8:9]
	v_mov_b64_e32 v[86:87], v[6:7]
	v_mov_b64_e32 v[84:85], v[4:5]
	v_mov_b64_e32 v[82:83], v[2:3]
	v_mov_b64_e32 v[80:81], v[0:1]
	s_mov_b32 s94, 0
	s_waitcnt vmcnt(0)
	s_branch .LBB0_787

; #define LAS __attribute__((address_space(3)))
; DI void at_stage1(LAS unsigned char* lds, const char* projb, int kcolB, int vcolB, int kt, int slot, int wid, unsigned lb0, unsigned lb1) {
;     const int kv = wid >> 2, sub0 = (wid & 3) * 4;
;     LAS unsigned char* dst = lds + slot * 32768 + kv * 16384 + sub0 * 1024;
;     const char* tb = projb + (size_t)kt * 64 * (INW * 2) + (kv ? vcolB : kcolB);
; #pragma unroll
;     for (int n = 0; n < 4; ++n) { const int sub = sub0 + n;
;         const size_t U = kv ? (size_t)((sub >> 1) * 8) * (INW * 2) + (size_t)((sub & 1) * 128) : (size_t)(sub * 4) * (INW * 2);
;         __builtin_amdgcn_global_load_lds((const unsigned*)(tb + U + ((n & 1) ? lb1 : lb0)), (LAS unsigned*)(dst + n * 1024), 16, 0, 0); }
; }
; DI void attn_unit_diff(const Ctx& C, int l, int b, int h, int j) {
;     ...
;     for (int sd = 0; sd < nt; ++sd) {
;         const int slot = sd % 3;
;         const bool staged = sd + 2 < nt;
;         if (staged) at_stage1(C.lds, projb, kcolB, vcolB, sd + 2, (sd + 2) % 3, wid, lb0, lb1);
.LBB0_791:
	s_mul_hi_u32 s57, s79, 0xaaaaaaab
	s_lshr_b32 s57, s57, 1
	s_mul_i32 s57, s57, 0x18000
	s_sub_i32 s58, s60, s57
	s_sub_i32 s59, s61, s57
	s_add_i32 s58, s49, s58
	v_lshl_add_u64 v[2:3], v[150:151], 0, s[52:53]
	s_sub_i32 s80, s4, s57
	s_add_i32 m0, s90, s58
	v_lshl_add_u64 v[4:5], v[2:3], 0, s[36:37]
	s_add_i32 s58, s49, s59
	s_sub_i32 s57, s5, s57
	global_load_lds_dwordx4 v[4:5], off
	v_lshl_add_u64 v[4:5], v[148:149], 0, s[52:53]
	s_add_i32 m0, s90, s58
	s_add_i32 s58, s49, s80
	global_load_lds_dwordx4 v[4:5], off
	v_lshl_add_u64 v[2:3], v[2:3], 0, s[24:25]
	s_add_i32 m0, s90, s58
	s_add_i32 s57, s49, s57
	v_xor_b32_e32 v2, s101, v2
	global_load_lds_dwordx4 v[2:3], off
	v_lshl_add_u64 v[2:3], v[146:147], 0, s[52:53]
	s_add_i32 m0, s90, s57
	s_nop 0
	v_xor_b32_e32 v2, s101, v2
	global_load_lds_dwordx4 v[2:3], off
	s_cmp_gt_u32 s94, s67
	s_cbranch_scc1 .LBB0_789

; #define LAS __attribute__((address_space(3)))
; #define AT_BAR() asm volatile("s_waitcnt vmcnt(0) lgkmcnt(0)\n\ts_barrier" ::: "memory")
; DI void at_stage1(LAS unsigned char* lds, const char* projb, int kcolB, int vcolB, int kt, int slot, int wid, unsigned lb0, unsigned lb1) {
;     const int kv = wid >> 2, sub0 = (wid & 3) * 4;
;     LAS unsigned char* dst = lds + slot * 32768 + kv * 16384 + sub0 * 1024;
;     const char* tb = projb + (size_t)kt * 64 * (INW * 2) + (kv ? vcolB : kcolB);
; #pragma unroll
;     for (int n = 0; n < 4; ++n) { const int sub = sub0 + n;
;         const size_t U = kv ? (size_t)((sub >> 1) * 8) * (INW * 2) + (size_t)((sub & 1) * 128) : (size_t)(sub * 4) * (INW * 2);
;         __builtin_amdgcn_global_load_lds((const unsigned*)(tb + U + ((n & 1) ? lb1 : lb0)), (LAS unsigned*)(dst + n * 1024), 16, 0, 0); }
; }
; DI void attn_unit_diff(const Ctx& C, int l, int b, int h, int j) {
;     ...
;     AT_BAR();
;     unsigned lb0, lb1;
;     { const int kv = wid >> 2;
;       if (kv == 0) { const int rl = lane >> 4, cp = lane & 15; lb0 = (unsigned)(rl * (INW * 2) + ((cp ^ (rl & 7)) * 16)); lb1 = (unsigned)(rl * (INW * 2) + ((cp ^ ((4 + rl) & 7)) * 16)); }
;       else { lb0 = (unsigned)(((lane & 31) >> 2) * (INW * 2) + ((lane >> 5) * 32 + (lane & 3) * 8) * 2); lb1 = lb0; } }
;     at_stage1(C.lds, projb, kcolB, vcolB, 0, 0, wid, lb0, lb1);
;     at_stage1(C.lds, projb, kcolB, vcolB, 1, 1, wid, lb0, lb1);
;     __builtin_amdgcn_sched_barrier(0);
;     bf16x8 qr[8];
;     { const bf16_t* qp = proj + (rowb + qpos) * INW + qcol + 8 * hi;
; #pragma unroll
;       for (int s = 0; s < KS; ++s) qr[s] = *(const bf16x8*)(qp + 16 * s); }
;     for (int i = wid * 64 + lane; i < TABB_N; i += NTHREADS) tabl[i] = tabg[i];
.LBB0_816:
	v_mov_b32_e32 v154, v153
	s_waitcnt vmcnt(0) lgkmcnt(0)
	s_barrier
	v_readlane_b32 s48, v252, 24
	v_readlane_b32 s49, v252, 25
	v_and_b32_e32 v155, 31, v154
	s_mov_b64 s[58:59], -1
	s_and_b64 vcc, exec, s[48:49]
	s_waitcnt vmcnt(0)
	v_lshlrev_b32_e32 v8, 3, v154
	s_cbranch_vccz .LBB0_818
	v_lshrrev_b32_e32 v0, 2, v155
	v_and_b32_e32 v2, 0x7fffffe0, v154
	s_mov_b32 s101, 0
	v_mul_u32_u24_e32 v0, 0x3000, v0
	v_and_or_b32 v2, v8, 24, v2
	v_lshl_add_u32 v2, v2, 1, v0
	s_mov_b64 s[58:59], 0
.LBB0_818:
	s_movk_i32 s48, 0x2800
	s_andn2_b64 vcc, exec, s[58:59]
	v_readlane_b32 s49, v252, 31
	v_readlane_b32 s52, v252, 30
	v_mov_b32_e32 v0, v2
	s_cbranch_vccnz .LBB0_820
	v_ashrrev_i32_e32 v0, 4, v154
	v_and_b32_e32 v2, 15, v154
	v_mul_lo_u32 v3, v0, s17
	s_movk_i32 s101, 0x80
	v_bitop3_b32 v0, v0, v2, 7 bitop3:0x6c
	v_lshlrev_b32_e32 v2, 4, v0
	v_or_b32_e32 v0, v2, v3
	v_bitop3_b32 v2, v2, 64, v3 bitop3:0x36
	s_movk_i32 s48, 0x2000
	v_readlane_b32 s49, v252, 32
	v_readlane_b32 s52, v252, 29
.LBB0_820:
	s_lshl_b32 s55, s6, 7
	v_readlane_b32 s57, v252, 23
	s_or_b32 s55, s55, s57
	s_or_b32 s11, s48, s11
	s_add_u32 s15, s15, s11
	s_addc_u32 s16, s16, 0
	s_add_u32 s58, s15, s21
	v_readlane_b32 s57, v253, 58
	s_addc_u32 s59, s16, 0
	s_mov_b32 m0, s57
	v_lshl_add_u64 v[4:5], s[58:59], 0, v[0:1]
	global_load_lds_dwordx4 v0, s[58:59]
	s_add_u32 s58, s15, s52
	s_addc_u32 s59, s16, 0
	s_mov_b32 m0, s82
	s_mov_b64 s[66:67], 0x18000
	global_load_lds_dwordx4 v2, s[58:59]
	s_add_u32 s58, s15, s49
	s_addc_u32 s59, s16, 0
	v_lshl_add_u64 v[4:5], v[4:5], 0, s[66:67]
	s_mov_b32 m0, s83
	s_add_u32 s11, s31, s11
	v_xor_b32_e32 v4, s101, v4
	global_load_lds_dwordx4 v[4:5], off
	s_mov_b32 m0, s84
	s_addc_u32 s15, s35, 0
	v_xor_b32_e32 v6, s101, v2
	global_load_lds_dwordx4 v6, s[58:59]
	s_add_u32 s58, s11, s21
	s_addc_u32 s59, s15, 0
	s_mov_b32 m0, s85
	v_lshl_add_u64 v[4:5], s[58:59], 0, v[0:1]
	global_load_lds_dwordx4 v0, s[58:59]
	s_add_u32 s58, s11, s52
	s_addc_u32 s59, s15, 0
	s_mov_b32 m0, s86
	v_lshl_add_u64 v[4:5], v[4:5], 0, s[66:67]
	global_load_lds_dwordx4 v2, s[58:59]
	s_mov_b32 m0, s87
	s_add_u32 s58, s11, s49
	v_xor_b32_e32 v4, s101, v4
	global_load_lds_dwordx4 v[4:5], off
	s_addc_u32 s59, s15, 0
	s_mov_b32 m0, s93
	v_ashrrev_i32_e32 v156, 5, v154
	v_xor_b32_e32 v6, s101, v2
	global_load_lds_dwordx4 v6, s[58:59]
	v_or_b32_e32 v3, s55, v155
	v_or_b32_e32 v3, s74, v3
	v_mov_b64_e32 v[4:5], s[46:47]
	v_mad_u64_u32 v[4:5], s[58:59], v3, s17, v[4:5]
	v_mad_i32_i24 v5, s75, v195, v5
	s_mov_b32 s79, s53
	v_lshlrev_b32_e32 v144, 3, v156
	v_lshl_add_u64 v[4:5], v[4:5], 0, s[78:79]
	v_ashrrev_i32_e32 v145, 31, v144
	v_lshl_add_u64 v[4:5], v[144:145], 1, v[4:5]
	global_load_dwordx4 v[128:131], v[4:5], off
	global_load_dwordx4 v[132:135], v[4:5], off offset:32
	global_load_dwordx4 v[136:139], v[4:5], off offset:64
	global_load_dwordx4 v[140:143], v[4:5], off offset:96
	v_readlane_b32 s11, v251, 4
	s_nop 1
	v_add_u32_e32 v4, s11, v154
	s_movk_i32 s11, 0x280
	v_cmp_gt_i32_e32 vcc, s11, v4
	s_and_saveexec_b64 s[58:59], vcc
	s_cbranch_execz .LBB0_828
	v_max_i32_e32 v3, 0x80, v4
	v_sub_u32_e32 v3, v3, v4
	v_add_u32_e32 v3, 0x1ff, v3
	s_movk_i32 s11, 0x1ff
	v_cmp_lt_u32_e32 vcc, s11, v3
	s_mov_b64 s[80:81], -1
	s_and_saveexec_b64 s[78:79], vcc
	s_cbranch_execz .LBB0_825
	v_lshrrev_b32_e32 v3, 9, v3
	v_add_u32_e32 v3, 1, v3
	v_and_b32_e32 v9, 0xfffffe, v3
	v_add_u32_e32 v5, 0x200, v4
	v_readlane_b32 s11, v253, 22
	s_mov_b64 s[80:81], 0
	v_mov_b32_e32 v11, v9
	v_lshl_add_u32 v10, v154, 2, s11
	v_mov_b64_e32 v[6:7], v[4:5]

; #define LAS __attribute__((address_space(3)))
;     __device__ __forceinline__ void init(const void* A_, const void* B_, int lda_, int ldb_, int M, unsigned mask_, int G_, int c_) { A = (const char*)A_; B = (const char*)B_; lda = lda_; ldb = ldb_; nM = M / BM; mask = mask_; nN = __builtin_popcount(mask_); nwg = nM * nN; G = G_; c = c_; }
;     __device__ __forceinline__ void init(f32x4 (&acc)[2][2][4][2], const Unit& u, int wr, int wc, int fr, int fq) const { u32x4 old[2][4][2]; init_load(old, u, wr, wc, fr, fq); init_finish(acc, old); }
; DI int at_v_rd_base(int lane) { return ((lane & 3) << 3) | (((lane >> 2) & 3) << 6) | (((lane >> 4) & 1) << 5) | (((lane >> 5) & 1) << 8); }
; template <int OFF> DI s16x4 at_tr_read(int vb) { s16x4 r; asm volatile("ds_read_b64_tr_b16 %0, %1 offset:%2" : "=&v"(r) : "v"(vb), "i"(OFF) : "memory"); return r; }
; DI unsigned at_cvtpk(float lo, float hi) { unsigned r; asm volatile("v_cvt_pk_bf16_f32 %0, %1, %2" : "=v"(r) : "v"(lo), "v"(hi)); return r; }
; template <int KS> DI void at_qk(f32x16& p0, f32x16& p1, LAS const unsigned char* Kt, int mapB, const bf16x8 (&qr)[8], float init, int r32, int hi) {
; #pragma unroll
;     for (int i = 0; i < 16; ++i) { p0[i] = init; p1[i] = init; }
;     bf16x8 kb[KS][2];
; #pragma unroll
;     for (int d0 = 0; d0 < KS; ++d0) { const int cb = mapB + (d0 * 16 + hi * 8) * 2;
;         kb[d0][0] = *(const LAS bf16x8*)(Kt + AT_KSWZ(r32, cb)); kb[d0][1] = *(const LAS bf16x8*)(Kt + AT_KSWZ(32 + r32, cb)); }
; DI void attn_unit_diff(const Ctx& C, int l, int b, int h, int j) {
;     ...
;     f32x16 o[4], ol = {}; float m_run = 0.f; bool first = true;
; #pragma unroll
;     for (int d0 = 0; d0 < 4; ++d0) o[d0] = f32x16{};
;     const bf16x8 ones = {16256, 16256, 16256, 16256, 16256, 16256, 16256, 16256};
;     asm volatile("s_waitcnt vmcnt(0) lgkmcnt(0)\n\ts_barrier" ::: "memory");
;     const float cfar = tabl[0];
;     const int vrd = at_v_rd_base(lane);
;     for (int sd = 0; sd < nt; ++sd) {
;         const int slot = sd % 3;
.LBB0_828:
	s_or_b64 exec, exec, s[58:59]
	s_and_b32 s11, s22, 15
	s_waitcnt vmcnt(0) lgkmcnt(0)
	s_barrier
	v_mov_b32_e32 v4, s50
	s_lshl_b32 s6, s6, 1
	v_readlane_b32 s7, v252, 22
	s_lshl_b32 s31, s11, 7
	s_lshl_b32 s11, s11, 16
	s_waitcnt lgkmcnt(0)
	ds_read_b32 v158, v4
	v_and_b32_e32 v4, 24, v8
	v_and_b32_e32 v7, 0x100, v8
	v_lshlrev_b32_e32 v8, 4, v156
	v_readlane_b32 s15, v252, 26
	v_readlane_b32 s35, v252, 23
	v_mov_b32_e32 v3, v1
	s_or_b32 s7, s6, s7
	s_add_i32 s11, s11, 0x10000
	v_lshlrev_b32_e32 v145, 4, v154
	v_add_u32_e32 v9, s15, v8
	v_lshlrev_b32_e32 v11, 4, v155
	v_lshlrev_b32_e32 v15, 2, v154
	s_add_i32 s16, s55, 0xfffffe90
	s_or_b32 s31, s35, s31
	s_add_i32 s52, s48, s28
	v_and_b32_e32 v5, 0xc0, v145
	v_lshlrev_b32_e32 v6, 1, v154
	v_lshlrev_b32_e32 v10, 8, v155
	v_and_b32_e32 v11, 0xf0, v11
	v_add_u32_e32 v14, 0x60, v9
	v_xor_b32_e32 v157, 0x80, v15
	v_add_lshl_u32 v15, s31, v155, 2
	v_lshl_add_u64 v[2:3], s[42:43], 0, v[2:3]
	s_add_u32 s42, s96, s42
	v_and_b32_e32 v6, 32, v6
	v_add_u32_e32 v12, 32, v9
	v_add_u32_e32 v13, 64, v9
	v_sub_u32_e32 v159, v8, v15
	v_add3_u32 v5, v7, s91, v5
	v_xad_u32 v164, v14, v11, v10
	s_addc_u32 s43, s89, s43
	v_mov_b32_e32 v14, v1
	v_mov_b32_e32 v15, v1
	v_add3_u32 v160, v5, v6, v4
	v_xad_u32 v161, v9, v11, v10
	v_xad_u32 v162, v12, v11, v10
	v_xad_u32 v163, v13, v11, v10
	v_lshl_add_u64 v[146:147], s[70:71], 0, v[2:3]
	v_lshl_add_u64 v[148:149], s[72:73], 0, v[2:3]
	v_lshl_add_u64 v[150:151], s[42:43], 0, v[0:1]
	v_mov_b32_e32 v0, v1
	v_mov_b32_e32 v2, v1
	v_mov_b32_e32 v3, v1
	v_mov_b32_e32 v4, v1
	v_mov_b32_e32 v5, v1
	v_mov_b32_e32 v6, v1
	v_mov_b32_e32 v7, v1
	v_mov_b32_e32 v8, v1
	v_mov_b32_e32 v9, v1
	v_mov_b32_e32 v10, v1
	v_mov_b32_e32 v11, v1
	v_mov_b32_e32 v12, v1
	v_mov_b32_e32 v13, v1
	v_mov_b64_e32 v[78:79], v[14:15]
	v_mov_b64_e32 v[62:63], v[14:15]
	v_mov_b64_e32 v[46:47], v[14:15]
	v_mov_b64_e32 v[30:31], v[14:15]
	v_mov_b64_e32 v[94:95], v[14:15]
	s_mov_b32 s15, 2
	s_mov_b32 s28, 0
	v_mov_b32_e32 v165, 0
	s_mov_b64 s[42:43], -1
	s_mov_b32 s31, 0
	v_mov_b64_e32 v[76:77], v[12:13]
	v_mov_b64_e32 v[74:75], v[10:11]
	v_mov_b64_e32 v[72:73], v[8:9]
	v_mov_b64_e32 v[70:71], v[6:7]
	v_mov_b64_e32 v[68:69], v[4:5]
	v_mov_b64_e32 v[66:67], v[2:3]
	v_mov_b64_e32 v[64:65], v[0:1]
	v_mov_b64_e32 v[60:61], v[12:13]
	v_mov_b64_e32 v[58:59], v[10:11]
	v_mov_b64_e32 v[56:57], v[8:9]
	v_mov_b64_e32 v[54:55], v[6:7]
	v_mov_b64_e32 v[52:53], v[4:5]
	v_mov_b64_e32 v[50:51], v[2:3]
	v_mov_b64_e32 v[48:49], v[0:1]
	v_mov_b64_e32 v[44:45], v[12:13]
	v_mov_b64_e32 v[42:43], v[10:11]
	v_mov_b64_e32 v[40:41], v[8:9]
	v_mov_b64_e32 v[38:39], v[6:7]
	v_mov_b64_e32 v[36:37], v[4:5]
	v_mov_b64_e32 v[34:35], v[2:3]
	v_mov_b64_e32 v[32:33], v[0:1]
	v_mov_b64_e32 v[28:29], v[12:13]
	v_mov_b64_e32 v[26:27], v[10:11]
	v_mov_b64_e32 v[24:25], v[8:9]
	v_mov_b64_e32 v[22:23], v[6:7]
	v_mov_b64_e32 v[20:21], v[4:5]
	v_mov_b64_e32 v[18:19], v[2:3]
	v_mov_b64_e32 v[16:17], v[0:1]
	v_mov_b64_e32 v[92:93], v[12:13]
	v_mov_b64_e32 v[90:91], v[10:11]
	v_mov_b64_e32 v[88:89], v[8:9]
	v_mov_b64_e32 v[86:87], v[6:7]
	v_mov_b64_e32 v[84:85], v[4:5]
	v_mov_b64_e32 v[82:83], v[2:3]
	v_mov_b64_e32 v[80:81], v[0:1]
	s_mov_b32 s35, 0
	s_waitcnt vmcnt(0)
	s_branch .LBB0_830

; #define LAS __attribute__((address_space(3)))
; DI void at_stage1(LAS unsigned char* lds, const char* projb, int kcolB, int vcolB, int kt, int slot, int wid, unsigned lb0, unsigned lb1) {
;     const int kv = wid >> 2, sub0 = (wid & 3) * 4;
;     LAS unsigned char* dst = lds + slot * 32768 + kv * 16384 + sub0 * 1024;
;     const char* tb = projb + (size_t)kt * 64 * (INW * 2) + (kv ? vcolB : kcolB);
; #pragma unroll
;     for (int n = 0; n < 4; ++n) { const int sub = sub0 + n;
;         const size_t U = kv ? (size_t)((sub >> 1) * 8) * (INW * 2) + (size_t)((sub & 1) * 128) : (size_t)(sub * 4) * (INW * 2);
;         __builtin_amdgcn_global_load_lds((const unsigned*)(tb + U + ((n & 1) ? lb1 : lb0)), (LAS unsigned*)(dst + n * 1024), 16, 0, 0); }
; }
; DI void attn_unit_diff(const Ctx& C, int l, int b, int h, int j) {
;     ...
;     for (int sd = 0; sd < nt; ++sd) {
;         const int slot = sd % 3;
;         const bool staged = sd + 2 < nt;
;         if (staged) at_stage1(C.lds, projb, kcolB, vcolB, sd + 2, (sd + 2) % 3, wid, lb0, lb1);
.LBB0_834:
	s_mul_hi_u32 s48, s15, 0xaaaaaaab
	s_lshr_b32 s48, s48, 1
	s_mul_i32 s48, s48, 0x18000
	s_sub_i32 s49, s60, s48
	s_sub_i32 s57, s61, s48
	s_add_i32 s49, s31, s49
	v_lshl_add_u64 v[2:3], v[150:151], 0, s[52:53]
	s_sub_i32 s58, s4, s48
	s_add_i32 m0, s90, s49
	v_lshl_add_u64 v[4:5], v[2:3], 0, s[36:37]
	s_add_i32 s49, s31, s57
	s_sub_i32 s48, s5, s48
	global_load_lds_dwordx4 v[4:5], off
	v_lshl_add_u64 v[4:5], v[148:149], 0, s[52:53]
	s_add_i32 m0, s90, s49
	s_add_i32 s49, s31, s58
	global_load_lds_dwordx4 v[4:5], off
	v_lshl_add_u64 v[2:3], v[2:3], 0, s[24:25]
	s_add_i32 m0, s90, s49
	s_add_i32 s48, s31, s48
	v_xor_b32_e32 v2, s101, v2
	global_load_lds_dwordx4 v[2:3], off
	v_lshl_add_u64 v[2:3], v[146:147], 0, s[52:53]
	s_add_i32 m0, s90, s48
	s_nop 0
	v_xor_b32_e32 v2, s101, v2
	global_load_lds_dwordx4 v[2:3], off
	s_cmp_gt_u32 s35, s7
	s_cbranch_scc1 .LBB0_832
